# P5b: shared-expert down-projection units remapped within each XCD group so workgroups with one routed unit fewer take 3 shared units and the others 1 (was 2 each); same unit set, each exactly once
# baseline (speedup 1.0000x reference)
; template <class PH>
; __device__ __forceinline__ void gemm_stream(unsigned char* smem, PH& ph) {
;     ...
;     bool have_iss = ph.desc(0, d_iss);
;     if (!have_iss) { if constexpr (PH::ROUND_SYNC) ph.round_finish(0); return; }
;     d_cmp = d_iss;
;     GPtrs P; GRows Q; Q.q0 = Q.q1 = Q.q2 = Q.q3 = 0;
;     ph.rows(d_iss, Q); ph.ptrs(d_iss, Q, P);
;     int iu = 0;
;     bool have_nxt = ph.desc(1, d_nxt);
;     if (have_nxt) ph.rows(d_nxt, Q);
;     int ik = 0, ink = ph.nk(d_iss), cnk = ink, issued = 0, computed = 0, cu = 0;
;     f32x4 acc[8][4];
;     ...
;     __syncthreads();
;     __device__ __forceinline__ bool desc(int i, Desc& d) const {
;         if (i < xm.nmine) {
;             const int lu = xm.lb + xm.nlb * i; int lo, ti; xmap_find(xm, lu >> 2, lo, ti);
;             d.kind = 0; d.e = xm.x + 8 * lo; d.nt = lu & 3; d.nrow = xm.cntl[lo] - ti * 256; d.lst = p.lists + (size_t)d.e * NLAT + ti * 256; d.mt = 0;
;             return true;
;         }
;         const int su = blockIdx.x + gridDim.x * (i - xm.nmine);
;         if (su >= 512) return false;
;         d.kind = 1; d.e = 0; d.nt = su & 3; d.nrow = 256; d.mt = su >> 2; d.lst = nullptr;
;         return true;
;     }
;     __device__ __forceinline__ void rows(const Desc& d, GRows& Q) const {
;         if (d.kind == 0) {
;             const int tid = otid();
;             const int r0 = s_row(tid, 0), r1 = s_row(tid, 1), r2 = s_row(tid, 2), r3 = s_row(tid, 3);
;             Q.q0 = d.lst[r0 < d.nrow ? r0 : 0]; Q.q1 = d.lst[r1 < d.nrow ? r1 : 0]; Q.q2 = d.lst[r2 < d.nrow ? r2 : 0]; Q.q3 = d.lst[r3 < d.nrow ? r3 : 0];
;         }
;     }
;     __device__ __forceinline__ void ptrs(const Desc& d, const GRows& Q, GPtrs& P) const {
;         const int tid = otid();
;         const bf16_t* a8 = (const bf16_t*)p.act;
;         if (d.kind == 0) {
;             P.a0 = a8 + (size_t)Q.q0 * 128 + s_ch(tid, 0); P.a1 = a8 + (size_t)Q.q1 * 128 + s_ch(tid, 1);
;             P.a2 = a8 + (size_t)Q.q2 * 128 + s_ch(tid, 2); P.a3 = a8 + (size_t)Q.q3 * 128 + s_ch(tid, 3);
;             ptrs_contig(P.b0, P.b1, P.b2, P.b3, (const bf16_t*)p.dT8 + (size_t)d.e * 131072, (size_t)d.nt * 256, 128);
;         } else {
;             ptrs_contig(P.a0, P.a1, P.a2, P.a3, a8, (size_t)NLAT * 8 + (size_t)d.mt * 256, 128);
;             ptrs_contig(P.b0, P.b1, P.b2, P.b3, (const bf16_t*)p.wsdT8, (size_t)d.nt * 256, 128);
;         }
.LBB0_1215:
	v_and_b32_e32 v254, 63, v0
	v_mov_b32_e32 v255, 0x20080
	ds_read_b32 v255, v255
	s_lshr_b32 s98, s2, 3
	s_and_b32 s99, s2, 7
	s_waitcnt lgkmcnt(0)
	v_readfirstlane_b32 s100, v255
	s_and_b32 s100, s100, 31
	s_sub_i32 s101, 32, s100
	s_sub_i32 s100, s98, s100
	v_mov_b32_e32 v255, s100
	v_mad_i32_i24 v253, v254, s101, v255
	s_lshl_b32 s101, s101, 1
	s_add_i32 s101, s101, s98
	v_lshl_add_u32 v255, v254, 5, s101
	v_add_u32_e32 v252, 0xffffffc0, v255
	v_cmp_gt_u32_e32 vcc, 2, v254
	s_nop 1
	v_cndmask_b32_e32 v253, v252, v253, vcc
	s_cmp_lt_i32 s100, 0
	s_cselect_b64 vcc, -1, 0
	s_nop 1
	v_cndmask_b32_e32 v253, v253, v255, vcc
	v_cmp_gt_u32_e32 vcc, 64, v253
	v_lshl_add_u32 v253, v253, 3, s99
	v_mov_b32_e32 v255, 0x200
	s_nop 0
	v_cndmask_b32_e32 v253, v255, v253, vcc
	s_nop 1
	v_readlane_b32 s98, v253, 0
	v_mov_b32_e32 v1, v0
	s_cmpk_gt_i32 s98, 0x1ff
	v_readfirstlane_b32 s0, v1
	s_cbranch_scc1 .LBB0_1237
	v_mov_b32_e32 v2, v0
	s_ashr_i32 s6, s98, 2
	v_mov_b32_e32 v10, v0
	s_ashr_i32 s1, s0, 1
	s_and_b32 s8, s0, 0xc0
	s_lshl_b32 s0, s0, 6
	s_ashr_i32 s7, s6, 31
	s_and_b32 s9, s1, 0xffffff80
	v_ashrrev_i32_e32 v2, 1, v10
	s_and_b32 s4, s98, 3
	s_and_b32 s3, s0, 0xfffff000
	s_lshl_b64 s[0:1], s[6:7], 8
	v_and_b32_e32 v11, 0xffffffe0, v2
	v_bfe_u32 v12, v10, 3, 3
	s_add_u32 s10, s0, 0x40000
	v_or_b32_e32 v4, v11, v12
	s_addc_u32 s11, s1, 0
	v_ashrrev_i32_e32 v5, 31, v4
	v_lshl_add_u64 v[2:3], s[10:11], 0, v[4:5]
	v_lshlrev_b64 v[2:3], 8, v[2:3]
	v_lshl_add_u64 v[6:7], s[28:29], 0, v[2:3]
	v_lshrrev_b32_e32 v2, 4, v10
	v_bitop3_b32 v2, v2, v10, 3 bitop3:0x6c
	v_lshrrev_b32_e32 v8, 3, v10
	v_lshlrev_b32_e32 v2, 4, v2
	v_and_b32_e32 v13, 6, v8
	v_and_b32_e32 v2, 0x70, v2
	v_mov_b32_e32 v3, 0
	v_or_b32_e32 v5, 8, v11
	v_lshl_add_u64 v[134:135], v[6:7], 0, v[2:3]
	v_or_b32_e32 v6, v5, v12
	v_or_b32_e32 v5, v5, v13
	v_lshrrev_b32_e32 v5, 1, v5
	v_xor_b32_e32 v5, v5, v10
	v_lshlrev_b32_e32 v5, 4, v5
	v_or_b32_e32 v4, 16, v4
	v_and_b32_e32 v8, 0x70, v5
	v_ashrrev_i32_e32 v5, 31, v4
	v_lshl_add_u64 v[4:5], s[10:11], 0, v[4:5]
	v_lshlrev_b64 v[4:5], 8, v[4:5]
	v_lshl_add_u64 v[4:5], s[28:29], 0, v[4:5]
	v_lshl_add_u64 v[138:139], v[4:5], 0, v[2:3]
	v_or_b32_e32 v2, 24, v11
	v_or_b32_e32 v4, v2, v12
	v_or_b32_e32 v2, v2, v13
	v_ashrrev_i32_e32 v5, 31, v4
	v_lshrrev_b32_e32 v2, 1, v2
	v_lshl_add_u64 v[4:5], s[10:11], 0, v[4:5]
	v_xor_b32_e32 v2, v2, v10
	v_lshlrev_b64 v[4:5], 8, v[4:5]
	v_lshlrev_b32_e32 v2, 4, v2
	v_lshl_add_u64 v[4:5], s[28:29], 0, v[4:5]
	v_and_b32_e32 v2, 0x70, v2
	v_mov_b32_e32 v10, v0
	v_ashrrev_i32_e32 v7, 31, v6
	v_lshl_add_u64 v[140:141], v[4:5], 0, v[2:3]
	v_lshl_add_u64 v[6:7], s[10:11], 0, v[6:7]
	v_ashrrev_i32_e32 v2, 1, v10
	v_and_b32_e32 v11, 0xffffffe0, v2
	v_bfe_u32 v13, v10, 3, 3
	v_lshlrev_b64 v[6:7], 8, v[6:7]
	v_or_b32_e32 v4, v11, v13
	s_mov_b32 s1, 0
	v_lshl_add_u64 v[6:7], s[28:29], 0, v[6:7]
	v_mov_b32_e32 v9, v3
	s_lshl_b32 s0, s4, 8
	v_ashrrev_i32_e32 v5, 31, v4
	v_lshrrev_b32_e32 v2, 4, v10
	v_lshl_add_u64 v[136:137], v[6:7], 0, v[8:9]
	v_lshl_add_u64 v[6:7], v[4:5], 0, s[0:1]
	v_bitop3_b32 v2, v2, v10, 3 bitop3:0x6c
	v_lshlrev_b64 v[6:7], 8, v[6:7]
	v_lshlrev_b32_e32 v2, 4, v2
	v_lshrrev_b32_e32 v12, 3, v10
	v_lshl_add_u64 v[6:7], s[34:35], 0, v[6:7]
	v_and_b32_e32 v2, 0x70, v2
	v_or_b32_e32 v5, 8, v11
	v_lshl_add_u64 v[142:143], v[6:7], 0, v[2:3]
	v_or_b32_e32 v6, v5, v13
	v_and_or_b32 v5, v12, 6, v5
	v_lshrrev_b32_e32 v5, 1, v5
	v_xor_b32_e32 v5, v5, v10
	v_lshlrev_b32_e32 v5, 4, v5
	v_or_b32_e32 v4, 16, v4
	v_and_b32_e32 v8, 0x70, v5
	v_ashrrev_i32_e32 v5, 31, v4
	v_lshl_add_u64 v[4:5], v[4:5], 0, s[0:1]
	v_lshlrev_b64 v[4:5], 8, v[4:5]
	v_readlane_b32 s7, v253, 1
	v_lshl_add_u64 v[4:5], s[34:35], 0, v[4:5]
	s_cmpk_lt_i32 s7, 0x200
	s_mov_b32 m0, s3
	v_ashrrev_i32_e32 v7, 31, v6
	v_lshl_add_u64 v[146:147], v[4:5], 0, v[2:3]
	v_or_b32_e32 v2, 24, v11
	s_cselect_b64 s[14:15], -1, 0
	s_barrier
	global_load_lds_dwordx4 v[134:135], off
	s_or_b32 m0, s3, 0x400
	v_lshl_add_u64 v[6:7], v[6:7], 0, s[0:1]
	v_or_b32_e32 v4, v2, v13
	v_or_b32_e32 v2, v2, v12
	global_load_lds_dwordx4 v[136:137], off
	s_or_b32 m0, s3, 0x800
	v_lshlrev_b64 v[6:7], 8, v[6:7]
	v_ashrrev_i32_e32 v5, 31, v4
	v_lshrrev_b32_e32 v2, 1, v2
	global_load_lds_dwordx4 v[138:139], off
	s_or_b32 m0, s3, 0xc00
	v_lshl_add_u64 v[6:7], s[34:35], 0, v[6:7]
	v_lshl_add_u64 v[4:5], v[4:5], 0, s[0:1]
	v_xor_b32_e32 v2, v2, v10
	global_load_lds_dwordx4 v[140:141], off
	s_add_i32 m0, s3, 0x8000
	v_lshl_add_u64 v[144:145], v[6:7], 0, v[8:9]
	v_lshlrev_b64 v[4:5], 8, v[4:5]
	v_lshlrev_b32_e32 v2, 4, v2
	global_load_lds_dwordx4 v[142:143], off
	s_add_i32 m0, s3, 0x8400
	v_lshl_add_u64 v[4:5], s[34:35], 0, v[4:5]
	v_and_b32_e32 v2, 0x70, v2
	global_load_lds_dwordx4 v[144:145], off
	s_add_i32 m0, s3, 0x8800
	v_lshl_add_u64 v[148:149], v[4:5], 0, v[2:3]
	global_load_lds_dwordx4 v[146:147], off
	s_add_i32 m0, s3, 0x8c00
	v_and_b32_e32 v2, 15, v1
	global_load_lds_dwordx4 v[148:149], off
	v_bfe_u32 v5, v1, 1, 3
	v_lshrrev_b32_e32 v1, 3, v1
	v_or_b32_e32 v4, s9, v2
	v_or_b32_e32 v2, s8, v2
	v_bitop3_b32 v1, v1, v5, 6 bitop3:0x6c
	v_lshlrev_b32_e32 v2, 7, v2
	v_lshlrev_b32_e32 v5, 4, v1
	s_and_b32 s0, s7, 3
	s_ashr_i32 s8, s7, 2
	v_lshlrev_b32_e32 v4, 7, v4
	v_or_b32_e32 v6, v2, v5
	s_mov_b32 s7, 0x8010
	s_cmpk_lt_i32 s9, 0x100
	s_mov_b32 s5, 1
	v_or_b32_e32 v1, v4, v5
	v_or_b32_e32 v150, 0x8000, v6
	v_bitop3_b32 v151, v4, 16, v5 bitop3:0x36
	v_bitop3_b32 v152, v2, s7, v5 bitop3:0x36
	s_cselect_b64 s[10:11], -1, 0
	s_add_i32 s7, s3, 0x10000
	s_mov_b64 s[16:17], -1
	s_mov_b64 s[20:21], 0
	v_mov_b32_e32 v153, 0x7f7f7f7f
	s_mov_b32 s12, 0x3b800000
	s_mov_b32 s13, 0
	s_mov_b32 s22, s1
	s_mov_b32 s9, 1
	s_mov_b32 s23, s1
	s_waitcnt vmcnt(0)
	s_branch .LBB0_1218

; __device__ __forceinline__ int otid() { int t = threadIdx.x; asm volatile("" : "+v"(t)); return t; }
; __device__ __forceinline__ int s_ch(int tid, int i) { const int r = s_row(tid, i); return ((tid & 7) ^ ((r >> 1) & 7)) * 8; }
;     __device__ __forceinline__ void ptrs(const Desc& d, const GRows& Q, GPtrs& P) const {
;         const int tid = otid();
;         const bf16_t* a8 = (const bf16_t*)p.act;
;         if (d.kind == 0) {
;             P.a0 = a8 + (size_t)Q.q0 * 128 + s_ch(tid, 0); P.a1 = a8 + (size_t)Q.q1 * 128 + s_ch(tid, 1);
;             P.a2 = a8 + (size_t)Q.q2 * 128 + s_ch(tid, 2); P.a3 = a8 + (size_t)Q.q3 * 128 + s_ch(tid, 3);
;             ptrs_contig(P.b0, P.b1, P.b2, P.b3, (const bf16_t*)p.dT8 + (size_t)d.e * 131072, (size_t)d.nt * 256, 128);
;         } else {
;             ptrs_contig(P.a0, P.a1, P.a2, P.a3, a8, (size_t)NLAT * 8 + (size_t)d.mt * 256, 128);
;             ptrs_contig(P.b0, P.b1, P.b2, P.b3, (const bf16_t*)p.wsdT8, (size_t)d.nt * 256, 128);
;         }
.LBB0_1225:
	s_waitcnt lgkmcnt(0)
	s_barrier
	s_andn2_b64 vcc, exec, s[16:17]
	s_cbranch_vccnz .LBB0_1229
	s_lshl_b32 s16, s5, 16
	s_and_b32 s20, s16, 0x10000
	s_lshl_b32 s16, s9, 6
	s_ashr_i32 s17, s16, 31
	s_lshl_b64 s[16:17], s[16:17], 1
	s_add_i32 s20, s3, s20
	v_lshl_add_u64 v[4:5], v[134:135], 0, s[16:17]
	s_mov_b32 m0, s20
	s_add_i32 s9, s9, 1
	global_load_lds_dwordx4 v[4:5], off
	v_lshl_add_u64 v[4:5], v[136:137], 0, s[16:17]
	s_add_i32 m0, s20, 0x400
	s_nop 0
	global_load_lds_dwordx4 v[4:5], off
	v_lshl_add_u64 v[4:5], v[138:139], 0, s[16:17]
	s_add_i32 m0, s20, 0x800
	s_nop 0
	global_load_lds_dwordx4 v[4:5], off
	v_lshl_add_u64 v[4:5], v[140:141], 0, s[16:17]
	s_add_i32 m0, s20, 0xc00
	s_nop 0
	global_load_lds_dwordx4 v[4:5], off
	v_lshl_add_u64 v[4:5], v[142:143], 0, s[16:17]
	s_add_i32 m0, s20, 0x8000
	s_nop 0
	global_load_lds_dwordx4 v[4:5], off
	v_lshl_add_u64 v[4:5], v[144:145], 0, s[16:17]
	s_add_i32 m0, s20, 0x8400
	s_nop 0
	global_load_lds_dwordx4 v[4:5], off
	v_lshl_add_u64 v[4:5], v[146:147], 0, s[16:17]
	s_add_i32 m0, s20, 0x8800
	s_nop 0
	global_load_lds_dwordx4 v[4:5], off
	v_lshl_add_u64 v[4:5], v[148:149], 0, s[16:17]
	s_add_i32 m0, s20, 0x8c00
	s_cmp_lg_u32 s9, 2
	global_load_lds_dwordx4 v[4:5], off
	s_mov_b64 s[16:17], -1
	s_cbranch_scc1 .LBB0_1232
	s_andn2_b64 vcc, exec, s[14:15]
	s_cbranch_vccnz .LBB0_1230
	v_mov_b32_e32 v2, v0
	v_mov_b32_e32 v140, v0
	s_ashr_i32 s9, s8, 31
	s_lshl_b64 s[14:15], s[8:9], 8
	v_ashrrev_i32_e32 v2, 1, v140
	v_and_b32_e32 v141, 0xffffffe0, v2
	v_bfe_u32 v142, v140, 3, 3
	s_add_u32 s14, s14, 0x40000
	v_or_b32_e32 v4, v141, v142
	s_addc_u32 s15, s15, 0
	v_lshrrev_b32_e32 v2, 3, v140
	v_ashrrev_i32_e32 v5, 31, v4
	v_lshl_add_u64 v[134:135], s[14:15], 0, v[4:5]
	v_and_b32_e32 v143, 6, v2
	v_or_b32_e32 v5, 8, v141
	v_or_b32_e32 v136, v5, v142
	v_or_b32_e32 v5, v5, v143
	v_lshrrev_b32_e32 v5, 1, v5
	v_xor_b32_e32 v5, v5, v140
	v_lshlrev_b32_e32 v5, 4, v5
	v_or_b32_e32 v4, 16, v4
	v_lshrrev_b32_e32 v2, 4, v140
	v_ashrrev_i32_e32 v137, 31, v136
	v_and_b32_e32 v138, 0x70, v5
	v_ashrrev_i32_e32 v5, 31, v4
	v_bitop3_b32 v2, v2, v140, 3 bitop3:0x6c
	v_lshl_add_u64 v[136:137], s[14:15], 0, v[136:137]
	v_lshl_add_u64 v[4:5], s[14:15], 0, v[4:5]
	v_lshlrev_b64 v[134:135], 8, v[134:135]
	v_lshlrev_b32_e32 v2, 4, v2
	v_lshlrev_b64 v[136:137], 8, v[136:137]
	v_lshlrev_b64 v[4:5], 8, v[4:5]
	v_lshl_add_u64 v[134:135], s[28:29], 0, v[134:135]
	v_and_b32_e32 v2, 0x70, v2
	v_lshl_add_u64 v[136:137], s[28:29], 0, v[136:137]
	v_mov_b32_e32 v139, v3
	v_lshl_add_u64 v[4:5], s[28:29], 0, v[4:5]
	v_lshl_add_u64 v[134:135], v[134:135], 0, v[2:3]
	v_lshl_add_u64 v[136:137], v[136:137], 0, v[138:139]
	v_lshl_add_u64 v[138:139], v[4:5], 0, v[2:3]
	v_or_b32_e32 v2, 24, v141
	v_or_b32_e32 v4, v2, v142
	v_or_b32_e32 v2, v2, v143
	v_ashrrev_i32_e32 v5, 31, v4
	v_lshrrev_b32_e32 v2, 1, v2
	v_lshl_add_u64 v[4:5], s[14:15], 0, v[4:5]
	v_xor_b32_e32 v2, v2, v140
	v_lshlrev_b64 v[4:5], 8, v[4:5]
	v_lshlrev_b32_e32 v2, 4, v2
	v_lshl_add_u64 v[4:5], s[28:29], 0, v[4:5]
	v_and_b32_e32 v2, 0x70, v2
	v_mov_b32_e32 v148, v0
	v_lshl_add_u64 v[140:141], v[4:5], 0, v[2:3]
	s_lshl_b64 s[14:15], s[0:1], 8
	v_ashrrev_i32_e32 v2, 1, v148
	v_and_b32_e32 v149, 0xffffffe0, v2
	v_bfe_u32 v155, v148, 3, 3
	v_or_b32_e32 v4, v149, v155
	v_ashrrev_i32_e32 v5, 31, v4
	v_lshrrev_b32_e32 v154, 3, v148
	v_lshl_add_u64 v[142:143], s[14:15], 0, v[4:5]
	v_or_b32_e32 v5, 8, v149
	v_or_b32_e32 v144, v5, v155
	v_and_or_b32 v5, v154, 6, v5
	v_lshrrev_b32_e32 v5, 1, v5
	v_xor_b32_e32 v5, v5, v148
	v_lshlrev_b32_e32 v5, 4, v5
	v_or_b32_e32 v4, 16, v4
	v_lshrrev_b32_e32 v2, 4, v148
	v_ashrrev_i32_e32 v145, 31, v144
	v_and_b32_e32 v146, 0x70, v5
	v_ashrrev_i32_e32 v5, 31, v4
	v_bitop3_b32 v2, v2, v148, 3 bitop3:0x6c
	v_lshl_add_u64 v[144:145], s[14:15], 0, v[144:145]
	v_lshl_add_u64 v[4:5], s[14:15], 0, v[4:5]
	v_lshlrev_b64 v[142:143], 8, v[142:143]
	v_lshlrev_b32_e32 v2, 4, v2
	v_lshlrev_b64 v[144:145], 8, v[144:145]
	v_lshlrev_b64 v[4:5], 8, v[4:5]
	s_add_i32 s4, s23, 2
	v_lshl_add_u64 v[142:143], s[34:35], 0, v[142:143]
	v_and_b32_e32 v2, 0x70, v2
	v_lshl_add_u64 v[144:145], s[34:35], 0, v[144:145]
	v_mov_b32_e32 v147, v3
	v_lshl_add_u64 v[4:5], s[34:35], 0, v[4:5]
	s_min_u32 s4, s4, 7
	v_lshl_add_u64 v[142:143], v[142:143], 0, v[2:3]
	v_lshl_add_u64 v[144:145], v[144:145], 0, v[146:147]
	v_lshl_add_u64 v[146:147], v[4:5], 0, v[2:3]
	v_or_b32_e32 v2, 24, v149
	v_readlane_b32 s4, v253, s4
	v_or_b32_e32 v4, v2, v155
	v_or_b32_e32 v2, v2, v154
	s_and_b32 s6, s4, 3
	s_ashr_i32 s9, s4, 2
	v_ashrrev_i32_e32 v5, 31, v4
	v_lshrrev_b32_e32 v2, 1, v2
	s_cmpk_lt_i32 s4, 0x200
	v_lshl_add_u64 v[4:5], s[14:15], 0, v[4:5]
	v_xor_b32_e32 v2, v2, v148
	s_cselect_b64 s[14:15], -1, 0
	v_lshlrev_b64 v[4:5], 8, v[4:5]
	v_lshlrev_b32_e32 v2, 4, v2
	s_and_b64 s[16:17], s[14:15], exec
	v_lshl_add_u64 v[4:5], s[34:35], 0, v[4:5]
	v_and_b32_e32 v2, 0x70, v2
	s_cselect_b32 s20, s9, s8
	s_cselect_b32 s21, s6, s0
	v_lshl_add_u64 v[148:149], v[4:5], 0, v[2:3]
	s_mov_b32 s9, 0
	s_mov_b64 s[16:17], -1
	s_mov_b32 s4, s0
	s_mov_b32 s6, s8
	s_mov_b32 s0, s21
	s_mov_b32 s8, s20
	s_branch .LBB0_1231

; #define LAS __attribute__((address_space(3)))
; #define RUNPH(bit, call) do { if ((PROBE_MASK >> (bit)) & 1) { const unsigned long long t0_ = __builtin_amdgcn_s_memrealtime(); call; \
;         const unsigned long long t1_ = __builtin_amdgcn_s_memrealtime(); while (__builtin_amdgcn_s_memrealtime() - t1_ < t1_ - t0_) __builtin_amdgcn_s_sleep(8); } else { call; } } while (0)
; __global__ void __launch_bounds__(512, 2) mk_fwd(KArgs ka) {
;     __shared__ __attribute__((aligned(16))) unsigned char smem[SMEM_BYTES];
;     const Params p = make_params(ka);
;     volatile LAS unsigned* xst = (volatile LAS unsigned*)(smem + SM_XB);
;     if (threadIdx.x == 0) { xst[0] = 0u; xst[1] = 0u; }
;     __syncthreads();
;     XcdBarrier xb = xcd_barrier_post((unsigned*)(ka.ws + OFF_BAR), xst);
;     RUNPH(0, phase0(p, smem, (unsigned*)(ka.ws + OFF_BAR) + XCD_BAR_WORDS + 64 * 18));
;     xcd_barrier(xb);
;     RUNPH(1, phase1a(p));
;     xcd_barrier(xb);
;     RUNPH(2, phase1b(p, smem));
;     xcd_barrier(xb);
;     RUNPH(3, phase2(p, smem, (unsigned*)(ka.ws + OFF_BAR) + XCD_BAR_WORDS + 64 * 17));
;     xcd_barrier(xb);
;     RUNPH(4, phase3(p, smem));
;     xcd_barrier(xb);
;     RUNPH(5, phase4a(p));
;     xcd_barrier(xb);
;     RUNPH(6, phase4b(p, smem));
;     xcd_barrier(xb);
;     RUNPH(10, phase4c(p, smem));
;     xcd_barrier(xb);
;     RUNPH(7, phase5a(p, smem, (unsigned*)(ka.ws + OFF_BAR) + XCD_BAR_WORDS));
;     xcd_barrier(xb);
;     RUNPH(8, phase5b(p, smem, (unsigned*)(ka.ws + OFF_BAR) + XCD_BAR_WORDS));
;     xcd_barrier(xb);
;     RUNPH(9, phase6(p));
; }
	.amdhsa_kernel _Z6mk_fwd5KArgs
		.amdhsa_group_segment_fixed_size 148480
		.amdhsa_private_segment_fixed_size 0
		.amdhsa_kernarg_size 480
		.amdhsa_user_sgpr_count 2
		.amdhsa_user_sgpr_dispatch_ptr 0
		.amdhsa_user_sgpr_queue_ptr 0
		.amdhsa_user_sgpr_kernarg_segment_ptr 1
		.amdhsa_user_sgpr_dispatch_id 0
		.amdhsa_user_sgpr_kernarg_preload_length 0
		.amdhsa_user_sgpr_kernarg_preload_offset 0
		.amdhsa_user_sgpr_private_segment_size 0
		.amdhsa_uses_dynamic_stack 0
		.amdhsa_enable_private_segment 0
		.amdhsa_system_sgpr_workgroup_id_x 1
		.amdhsa_system_sgpr_workgroup_id_y 0
		.amdhsa_system_sgpr_workgroup_id_z 0
		.amdhsa_system_sgpr_workgroup_info 0
		.amdhsa_system_vgpr_workitem_id 0
		.amdhsa_next_free_vgpr 256
		.amdhsa_next_free_sgpr 102
		.amdhsa_accum_offset 256
		.amdhsa_reserve_vcc 1
		.amdhsa_float_round_mode_32 0
		.amdhsa_float_round_mode_16_64 0
		.amdhsa_float_denorm_mode_32 3
		.amdhsa_float_denorm_mode_16_64 3
		.amdhsa_dx10_clamp 1
		.amdhsa_ieee_mode 1
		.amdhsa_fp16_overflow 0
		.amdhsa_tg_split 0
		.amdhsa_exception_fp_ieee_invalid_op 0
		.amdhsa_exception_fp_denorm_src 0
		.amdhsa_exception_fp_ieee_div_zero 0
		.amdhsa_exception_fp_ieee_overflow 0
		.amdhsa_exception_fp_ieee_underflow 0
		.amdhsa_exception_fp_ieee_inexact 0
		.amdhsa_exception_int_div_zero 0
	.end_amdhsa_kernel

; #define LAS __attribute__((address_space(3)))
; #define RUNPH(bit, call) do { if ((PROBE_MASK >> (bit)) & 1) { const unsigned long long t0_ = __builtin_amdgcn_s_memrealtime(); call; \
;         const unsigned long long t1_ = __builtin_amdgcn_s_memrealtime(); while (__builtin_amdgcn_s_memrealtime() - t1_ < t1_ - t0_) __builtin_amdgcn_s_sleep(8); } else { call; } } while (0)
; __global__ void __launch_bounds__(512, 2) mk_fwd(KArgs ka) {
;     __shared__ __attribute__((aligned(16))) unsigned char smem[SMEM_BYTES];
;     const Params p = make_params(ka);
;     volatile LAS unsigned* xst = (volatile LAS unsigned*)(smem + SM_XB);
;     if (threadIdx.x == 0) { xst[0] = 0u; xst[1] = 0u; }
;     __syncthreads();
;     XcdBarrier xb = xcd_barrier_post((unsigned*)(ka.ws + OFF_BAR), xst);
;     RUNPH(0, phase0(p, smem, (unsigned*)(ka.ws + OFF_BAR) + XCD_BAR_WORDS + 64 * 18));
;     xcd_barrier(xb);
;     RUNPH(1, phase1a(p));
;     xcd_barrier(xb);
;     RUNPH(2, phase1b(p, smem));
;     xcd_barrier(xb);
;     RUNPH(3, phase2(p, smem, (unsigned*)(ka.ws + OFF_BAR) + XCD_BAR_WORDS + 64 * 17));
;     xcd_barrier(xb);
;     RUNPH(4, phase3(p, smem));
;     xcd_barrier(xb);
;     RUNPH(5, phase4a(p));
;     xcd_barrier(xb);
;     RUNPH(6, phase4b(p, smem));
;     xcd_barrier(xb);
;     RUNPH(10, phase4c(p, smem));
;     xcd_barrier(xb);
;     RUNPH(7, phase5a(p, smem, (unsigned*)(ka.ws + OFF_BAR) + XCD_BAR_WORDS));
;     xcd_barrier(xb);
;     RUNPH(8, phase5b(p, smem, (unsigned*)(ka.ws + OFF_BAR) + XCD_BAR_WORDS));
;     xcd_barrier(xb);
;     RUNPH(9, phase6(p));
; }
amdhsa.kernels:
  - .agpr_count:     0
    .args:
      - .offset:         0
        .size:           224
        .value_kind:     by_value
      - .offset:         224
        .size:           4
        .value_kind:     hidden_block_count_x
      - .offset:         228
        .size:           4
        .value_kind:     hidden_block_count_y
      - .offset:         232
        .size:           4
        .value_kind:     hidden_block_count_z
      - .offset:         236
        .size:           2
        .value_kind:     hidden_group_size_x
      - .offset:         238
        .size:           2
        .value_kind:     hidden_group_size_y
      - .offset:         240
        .size:           2
        .value_kind:     hidden_group_size_z
      - .offset:         242
        .size:           2
        .value_kind:     hidden_remainder_x
      - .offset:         244
        .size:           2
        .value_kind:     hidden_remainder_y
      - .offset:         246
        .size:           2
        .value_kind:     hidden_remainder_z
      - .offset:         264
        .size:           8
        .value_kind:     hidden_global_offset_x
      - .offset:         272
        .size:           8
        .value_kind:     hidden_global_offset_y
      - .offset:         280
        .size:           8
        .value_kind:     hidden_global_offset_z
      - .offset:         288
        .size:           2
        .value_kind:     hidden_grid_dims
    .group_segment_fixed_size: 148480
    .kernarg_segment_align: 8
    .kernarg_segment_size: 480
    .language:       OpenCL C
    .language_version:
      - 2
      - 0
    .max_flat_workgroup_size: 512
    .name:           _Z6mk_fwd5KArgs
    .private_segment_fixed_size: 0
    .sgpr_count:     108
    .sgpr_spill_count: 50
    .symbol:         _Z6mk_fwd5KArgs.kd
    .uniform_work_group_size: 1
    .uses_dynamic_stack: false
    .vgpr_count:     256
    .vgpr_spill_count: 0
    .wavefront_size: 64
